# stagger XCD halves by ~8us at start of pool/merge/out/ple GEMM phases to de-burst epilogue traffic
# speedup vs baseline: 1.0360x; 1.0360x over previous
; #define LAS __attribute__((address_space(3)))
; __global__ void __launch_bounds__(NTHR, 2) fwd(Args args) {
;     ...
;     F.lds = (LAS unsigned char*)lds_raw; F.MISC = (volatile LAS unsigned*)(F.lds + MISC_OFF);
;     F.tid = threadIdx.x; F.lane = F.tid & 63; F.wave = __builtin_amdgcn_readfirstlane(F.tid >> 6);
;     F.G = gridDim.x; { const int bx = blockIdx.x; F.vcu = (F.G % 8 == 0) ? (bx % 8) * (F.G / 8) + bx / 8 : bx; }
;     F.ws = args.ws; F.ctl = (unsigned*)(args.ws + WS_CTL); F.out = args.out;
; #pragma unroll
;     for (int i = 0; i < 25; ++i) F.in[i] = args.in[i];
;     for (int u = F.tid; u < MISC_WORDS; u += NTHR) F.MISC[u] = 0u;
;     __syncthreads();
;     XcdBarrier bar; bar.bar = F.ctl + CW_BAR; bar.x = 0; bar.st = nullptr;
_Z3fwd4Args:
	s_load_dword s31, s[0:1], 0xe8
	s_mov_b64 s[24:25], s[0:1]
	s_add_u32 s0, s24, 0xe8
	s_addc_u32 s1, s25, 0
	v_readfirstlane_b32 s97, v0
	v_writelane_b32 v247, s0, 0
	s_mov_b32 s96, s2
	s_nop 0
	v_writelane_b32 v247, s1, 1
	s_waitcnt lgkmcnt(0)
	s_and_b32 s0, s31, 7
	s_cmp_lg_u32 s0, 0
	s_mov_b32 s0, s2
	v_writelane_b32 v247, s0, 2
	s_nop 1
	v_writelane_b32 v247, s1, 3
	s_cbranch_scc1 .LBB0_2
	v_readlane_b32 s2, v247, 2
	s_ashr_i32 s1, s2, 31
	s_lshr_b32 s1, s1, 29
	s_add_i32 s1, s2, s1
	s_mov_b32 s4, s2
	s_and_b32 s2, s1, -8
	s_ashr_i32 s0, s31, 3
	s_sub_i32 s2, s4, s2
	s_mul_i32 s0, s0, s2
	s_ashr_i32 s1, s1, 3
	s_add_i32 s96, s0, s1
	v_readlane_b32 s3, v247, 3

; template <class Epi, class Sched, bool GATHER, bool ALIGN_EPI = true, bool SP2 = true, bool REMAP64 = false>
; __device__ __forceinline__ void gemm_phase(LAS unsigned char* lds, const bf16* Ag, const bf16* Btg, const int K, const Sched& S, const Epi& E) {
;     const int tid = threadIdx.x, wid = __builtin_amdgcn_readfirstlane(tid >> 6), lane = tid & 63, wr = wid >> 2, wc = wid & 3, fr = lane & 15, fq = lane >> 4;
;     const int nt = K / BK;
;     unsigned voffA[2], voffB[2]; int RA[2], CA[2];
; #pragma unroll
;     for (int i = 0; i < 2; ++i) { int R, C; stage_rc(tid * 16 + i * 8192, R, C); const int Rb = REMAP64 ? 64 * (R >> 5) + perm32(R & 31) : (R & ~31) + perm32(R & 31);
;         voffA[i] = (unsigned)(R * K + C) * 2u; voffB[i] = (unsigned)(Rb * K + C) * 2u; RA[i] = R; CA[i] = C; }
;     const size_t kstep = (size_t)(BK * 2);
;     const size_t hstep = (size_t)HALF * K * 2;
;     const size_t hstepB = REMAP64 ? (size_t)32 * K * 2 : hstep;
;     const unsigned ldsw = (unsigned)wid * 1024u;
;     const int aoff = lds_byte(wr * 64 + fr, fq * 8), boff = lds_byte(wc * 32 + fr, fq * 8);
;     ...
;     Unit cur, nxt; int ui = 0;
;     if (!S.next(0, cur)) return;
;     f32x4 acc[2][2][4][2];
; #pragma unroll
;     for (int a = 0; a < 2; ++a)
; #pragma unroll
;         for (int b = 0; b < 2; ++b)
; #pragma unroll
;             for (int m = 0; m < 4; ++m)
; #pragma unroll
;                 for (int n = 0; n < 2; ++n) acc[a][b][m][n] = (f32x4){0.f, 0.f, 0.f, 0.f};
;     bf16x8 At[4][2], B0[2][2], B1[2][2];
;     unsigned vc[2][2], vn[2][2];
;     if (GATHER) { PG8_ROWOFFS(vc, cur); }
;     const char* cA = GATHER ? (const char*)Ag : (const char*)Ag + (size_t)cur.arow0 * K * 2; const char* cB = (const char*)Btg + S.boff(cur) * 2;
;     if constexpr (SP2) {
;         PG8_STAGE(PG8_SB(0, 0), cB, voffB); PG8_STAGE(PG8_SB(0, 1), cB + hstepB, voffB); PG8_STAGE_A(PG8_SA(0, 0), cA, vc, 0, 0); PG8_STAGE_A(PG8_SA(0, 1), cA, vc, 1, 0);
;         if (wr == 1) PG8_BAR;
;         PG8_WAIT_V(2); PG8_BAR;
; __global__ void __launch_bounds__(NTHR, 2) fwd(Args args) {
;     ...
;         } } else if (!(args.flags & 2)) {
;             pg8::DenseOrder S; S.init(T, D, D_POOL, F.G - NB * NH, (int)blockIdx.x - NB * NH); EpiPool E{GP, MP};
;             if (!(args.flags & 8)) pg8::gemm_phase<EpiPool, pg8::DenseOrder, false, true, true, true>(F.lds + RING_OFF, DBUF, WCOMB, D_POOL, S, E);
.LBB0_934:
	s_andn2_b64 vcc, exec, s[0:1]
	s_cbranch_vccnz .LBB0_970
	s_waitcnt vmcnt(0)
	v_readlane_b32 s98, v247, 2
	s_nop 3
	s_and_b32 s98, s98, 4
	s_cmp_eq_u32 s98, 0
	s_cbranch_scc1 .Lstag_pool
	s_sleep 127
	s_sleep 127
.Lstag_pool:
	v_lshrrev_b32_e32 v5, 1, v0
	v_and_b32_e32 v14, 24, v5
	v_lshrrev_b32_e32 v5, 5, v0
	v_lshlrev_b32_e32 v2, 4, v0
	v_and_b32_e32 v3, 32, v0
	v_and_b32_e32 v5, 4, v5
	v_bfe_u32 v6, v0, 2, 2
	v_lshrrev_b32_e32 v4, 2, v0
	v_bitop3_b32 v10, v2, v3, 48 bitop3:0x6c
	v_and_b32_e32 v11, 64, v0
	v_or3_b32 v5, v5, v6, v14
	v_or_b32_e32 v13, 0x2000, v2
	v_bfe_u32 v12, v0, 2, 4
	v_or_b32_e32 v3, v10, v11
	v_and_or_b32 v4, v4, 64, v5
	v_lshrrev_b32_e32 v2, 7, v13
	s_movk_i32 s0, 0x70
	s_lshr_b32 s6, s8, 6
	v_lshl_or_b32 v148, v4, 11, v3
	v_and_or_b32 v2, v2, s0, v12
	v_lshrrev_b32_e32 v4, 6, v13
	s_movk_i32 s0, 0xc0
	s_ashr_i32 s11, s10, 31
	s_ashr_i32 s53, s52, 31
	v_and_or_b32 v4, v4, s0, v5
	s_lshr_b32 s7, s8, 8
	s_lshl_b32 s63, s6, 10
	s_lshl_b64 s[0:1], s[10:11], 11
	s_lshl_b64 s[12:13], s[52:53], 19
	v_readlane_b32 s14, v247, 47
	v_readlane_b32 s15, v247, 48
	s_add_u32 s54, s14, s12
	s_addc_u32 s55, s15, s13
	s_add_i32 s53, s63, 0
	s_add_i32 m0, s53, 0x10000
	v_lshl_or_b32 v152, v4, 11, v3
	global_load_lds_dwordx4 v148, s[54:55]
	s_add_i32 m0, s53, 0x12000
	s_add_u32 s12, s54, 0x10000
	global_load_lds_dwordx4 v152, s[54:55]
	s_addc_u32 s13, s55, 0
	s_add_i32 m0, s53, 0x14000
	v_readlane_b32 s16, v247, 45
	global_load_lds_dwordx4 v148, s[12:13]
	s_add_i32 m0, s53, 0x16000
	v_readlane_b32 s17, v247, 46
	global_load_lds_dwordx4 v152, s[12:13]
	s_load_dwordx4 s[12:15], s[16:17], 0xc0
	v_lshrrev_b32_e32 v6, 3, v0
	v_and_or_b32 v6, v6, 48, v12
	v_lshl_or_b32 v146, v6, 11, v3
	s_mov_b32 m0, s53
	s_waitcnt lgkmcnt(0)
	s_add_u32 s56, s14, s0
	s_addc_u32 s57, s15, s1
	s_add_i32 s72, s53, 0x2000
	s_add_u32 s0, s56, 0x40000
	v_lshl_or_b32 v150, v2, 11, v3
	global_load_lds_dwordx4 v146, s[56:57]
	s_mov_b32 m0, s72
	s_addc_u32 s1, s57, 0
	s_add_i32 s73, s53, 0x4000
	global_load_lds_dwordx4 v150, s[56:57]
	s_mov_b32 m0, s73
	s_add_i32 s74, s53, 0x6000
	global_load_lds_dwordx4 v146, s[0:1]
	s_mov_b32 m0, s74
	v_mov_b32_e32 v155, 0
	global_load_lds_dwordx4 v150, s[0:1]
	v_mov_b32_e32 v149, v155
	v_mov_b32_e32 v153, v155
	v_mov_b32_e32 v147, v155
	v_mov_b32_e32 v151, v155
	s_cmp_eq_u32 s7, 1
	s_mov_b32 s75, 0
	v_lshl_add_u64 v[8:9], s[54:55], 0, v[148:149]
	v_lshl_add_u64 v[6:7], s[54:55], 0, v[152:153]
	v_lshl_add_u64 v[2:3], s[56:57], 0, v[146:147]
	s_cselect_b64 s[0:1], -1, 0
	s_cmp_lg_u32 s7, 1
	v_lshl_add_u64 v[4:5], s[56:57], 0, v[150:151]
	s_cbranch_scc1 .LBB0_937
	s_barrier

; template <class Epi, class Sched, bool GATHER, bool ALIGN_EPI = true, bool SP2 = true, bool REMAP64 = false>
; __device__ __forceinline__ void gemm_phase(LAS unsigned char* lds, const bf16* Ag, const bf16* Btg, const int K, const Sched& S, const Epi& E) {
;     ...
;             const bool hi = RP && (fr >= 8); const int rsh = hi ? -8 : 0, citx = hi ? cit + 32 : cit;
;             typename Epi::Pre pq[2];
;             { const int r0_ = wr * 64 + fr; pq[0] = E.pre(cur, (r0_ < cur.nrows ? r0_ : cur.nrows - 1) + rsh, citx); }
; #pragma unroll
;             for (int gq = 0; gq < 8; ++gq) { const int ai = gq >> 2, m = gq & 3, r = ai * HALF + wr * 64 + m * 16 + fr;
;                 if (gq + 1 < 8) { const int rn = ((gq + 1) >> 2) * HALF + wr * 64 + ((gq + 1) & 3) * 16 + fr; pq[(gq + 1) & 1] = E.pre(cur, (rn < cur.nrows ? rn : cur.nrows - 1) + rsh, citx); }
;                 __builtin_amdgcn_sched_barrier(0);
;                 if (r < cur.nrows) { float v0[8], v1[8];
; #pragma unroll
;                     for (int i = 0; i < 4; ++i) { v0[i] = acc[ai][0][m][0][i]; v0[4 + i] = acc[ai][0][m][1][i]; v1[i] = acc[ai][1][m][0][i]; v1[4 + i] = acc[ai][1][m][1][i]; }
;                     if constexpr (RP) {
; #pragma unroll
;                         for (int i = 0; i < 8; ++i) { const float snd = hi ? v0[i] : v1[i];
;                             const float rcv = __builtin_bit_cast(float, __builtin_amdgcn_update_dpp(0, __builtin_bit_cast(int, snd), 0x128, 0xf, 0xf, false));
;                             if (hi) v0[i] = rcv; else v1[i] = rcv; } }
;                     E.post(cur, r + rsh, citx, v0, v1, pq[gq & 1]); }
;     __device__ __forceinline__ Pre pre(const Unit& u, int r, int cit) const { const size_t off = (size_t)(u.arow0 + r) * D + u.pn * 256 + cit; return Pre{__builtin_nontemporal_load((const v4u*)(gp + off)), __builtin_nontemporal_load((const v4u*)(gp + off + (size_t)8 * D))}; }
;     __device__ __forceinline__ void post(const Unit& u, int r, int cit, const float* v0, const float* v1, const Pre& p) const {
;         const size_t off = (size_t)(u.arow0 + r) * D + u.pn * 256 + cit; float g0[8], g1[8], a[8], b[8]; unpack8bf(p.g0, g0); unpack8bf(p.g1, g1);
; #pragma unroll
;         for (int i = 0; i < 8; ++i) { a[i] = g0[i] * v0[i]; b[i] = g1[i] * v1[i]; }
;         store8bf(mp + off, a); store8bf(mp + off + (size_t)8 * D, b);
;     }
.LBB0_950:
	v_add_u32_e32 v130, s10, v176
	v_ashrrev_i32_e32 v131, 31, v130
	s_lshl_b32 s54, s52, 8
	s_ashr_i32 s55, s54, 31
	v_lshlrev_b64 v[130:131], 12, v[130:131]
	v_lshl_add_u64 v[130:131], s[48:49], 0, v[130:131]
	s_lshl_b64 s[54:55], s[54:55], 1
	v_lshl_add_u64 v[130:131], v[130:131], 0, s[54:55]
	v_lshl_add_u64 v[130:131], v[130:131], 0, v[154:155]
	v_add_co_u32_e32 v132, vcc, 0x8000, v130
	v_add_u32_e32 v188, s10, v175
	s_nop 0
	v_addc_co_u32_e32 v133, vcc, 0, v131, vcc
	global_load_dwordx4 v[142:145], v[130:131], off nt
	global_load_dwordx4 v[138:141], v[132:133], off nt
	v_add_u32_e32 v130, v188, v177
	v_ashrrev_i32_e32 v131, 31, v130
	v_lshl_add_u64 v[172:173], v[156:157], 0, s[54:55]
	v_lshlrev_b64 v[130:131], 12, v[130:131]
	v_lshl_add_u64 v[130:131], v[172:173], 0, v[130:131]
	v_add_co_u32_e32 v132, vcc, 0x8000, v130
	v_lshl_add_u64 v[168:169], v[158:159], 0, s[54:55]
	s_nop 0
	v_addc_co_u32_e32 v133, vcc, 0, v131, vcc
	global_load_dwordx4 v[134:137], v[130:131], off nt
	s_nop 0
	global_load_dwordx4 v[130:133], v[132:133], off nt
	v_add_u32_e32 v187, v188, v171
	s_and_b64 vcc, exec, s[16:17]
	s_cbranch_vccz .LBB0_952
	v_cndmask_b32_e64 v189, v118, v126, s[6:7]
	v_mov_b32_e32 v190, v155
	s_waitcnt vmcnt(0)
	v_lshlrev_b32_e32 v194, 16, v139
	v_and_b32_e32 v139, 0xffff0000, v139
	v_mov_b32_dpp v190, v189 row_ror:8 row_mask:0xf bank_mask:0xf
	v_cndmask_b32_e64 v189, v119, v127, s[6:7]
	v_cndmask_b32_e64 v126, v126, v190, s[6:7]
	v_cndmask_b32_e64 v118, v190, v118, s[6:7]
	v_mov_b32_e32 v190, v155
	v_lshlrev_b32_e32 v195, 16, v140
	v_and_b32_e32 v140, 0xffff0000, v140
	v_mov_b32_dpp v190, v189 row_ror:8 row_mask:0xf bank_mask:0xf
	v_cndmask_b32_e64 v189, v120, v128, s[6:7]
	v_cndmask_b32_e64 v127, v127, v190, s[6:7]
	v_cndmask_b32_e64 v119, v190, v119, s[6:7]
	v_mov_b32_e32 v190, v155
	v_lshlrev_b32_e32 v191, 16, v144
	v_and_b32_e32 v144, 0xffff0000, v144
	v_mov_b32_dpp v190, v189 row_ror:8 row_mask:0xf bank_mask:0xf
	v_cndmask_b32_e64 v189, v121, v129, s[6:7]
	v_cndmask_b32_e64 v128, v128, v190, s[6:7]
	v_cndmask_b32_e64 v120, v190, v120, s[6:7]
	v_mov_b32_e32 v190, v155
	v_lshlrev_b32_e32 v192, 16, v145
	v_and_b32_e32 v145, 0xffff0000, v145
	v_mov_b32_dpp v190, v189 row_ror:8 row_mask:0xf bank_mask:0xf
	v_cndmask_b32_e64 v189, v114, v122, s[6:7]
	v_cndmask_b32_e64 v129, v129, v190, s[6:7]
	v_cndmask_b32_e64 v121, v190, v121, s[6:7]
	v_mov_b32_e32 v190, v155
	v_mul_f32_e32 v121, v121, v139
	v_lshlrev_b32_e32 v193, 16, v138
	v_mov_b32_dpp v190, v189 row_ror:8 row_mask:0xf bank_mask:0xf
	v_cndmask_b32_e64 v189, v115, v123, s[6:7]
	v_cndmask_b32_e64 v122, v122, v190, s[6:7]
	v_cndmask_b32_e64 v114, v190, v114, s[6:7]
	v_mov_b32_e32 v190, v155
	v_mul_f32_e32 v139, v114, v195
	v_add_u32_e32 v114, s76, v187
	v_mov_b32_dpp v190, v189 row_ror:8 row_mask:0xf bank_mask:0xf
	v_cndmask_b32_e64 v189, v116, v124, s[6:7]
	v_cndmask_b32_e64 v123, v123, v190, s[6:7]
	v_cndmask_b32_e64 v115, v190, v115, s[6:7]
	v_mov_b32_e32 v190, v155
	v_mul_f32_e32 v140, v115, v140
	v_ashrrev_i32_e32 v115, 31, v114
	v_mov_b32_dpp v190, v189 row_ror:8 row_mask:0xf bank_mask:0xf
	v_cndmask_b32_e64 v189, v117, v125, s[6:7]
	v_cndmask_b32_e64 v124, v124, v190, s[6:7]
	v_cndmask_b32_e64 v116, v190, v116, s[6:7]
	v_mov_b32_e32 v190, v155
	v_and_b32_e32 v138, 0xffff0000, v138
	v_lshlrev_b32_e32 v196, 16, v141
	v_mov_b32_dpp v190, v189 row_ror:8 row_mask:0xf bank_mask:0xf
	v_cndmask_b32_e64 v125, v125, v190, s[6:7]
	v_cndmask_b32_e64 v117, v190, v117, s[6:7]
	v_lshlrev_b32_e32 v189, 16, v142
	v_and_b32_e32 v142, 0xffff0000, v142
	v_lshlrev_b32_e32 v190, 16, v143
	v_and_b32_e32 v143, 0xffff0000, v143
	v_and_b32_e32 v141, 0xffff0000, v141
	v_mul_f32_e32 v126, v126, v189
	v_mul_f32_e32 v127, v127, v142
	v_mul_f32_e32 v128, v128, v190
	v_mul_f32_e32 v129, v129, v143
	v_mul_f32_e32 v122, v122, v191
	v_mul_f32_e32 v123, v123, v144
	v_mul_f32_e32 v124, v124, v192
	v_mul_f32_e32 v125, v125, v145
	v_lshlrev_b64 v[114:115], 12, v[114:115]
	v_mul_f32_e32 v189, v118, v193
	v_mul_f32_e32 v138, v119, v138
	v_mul_f32_e32 v142, v116, v196
	v_mul_f32_e32 v141, v117, v141
	v_lshl_add_u64 v[118:119], v[168:169], 0, v[114:115]
	v_cvt_pk_bf16_f32 v114, v126, v127
	v_cvt_pk_bf16_f32 v115, v128, v129
	v_cvt_pk_bf16_f32 v116, v122, v123
	v_cvt_pk_bf16_f32 v117, v124, v125
	v_mul_f32_e32 v120, v120, v194
	global_store_dwordx4 v[118:119], v[114:117], off
	v_add_co_u32_e32 v118, vcc, 0x8000, v118
	s_nop 0
	v_cvt_pk_bf16_f32 v114, v189, v138
	v_cvt_pk_bf16_f32 v115, v120, v121
	v_cvt_pk_bf16_f32 v116, v139, v140
	v_cvt_pk_bf16_f32 v117, v142, v141
	v_addc_co_u32_e32 v119, vcc, 0, v119, vcc
	global_store_dwordx4 v[118:119], v[114:117], off

;     __device__ __forceinline__ size_t boff(const Unit& u) const { return (size_t)u.pn * 256 * K; }
;     __device__ __forceinline__ size_t boff(const Unit& u) const { return Dn.boff(u); }
; template <class Epi, class Sched, bool GATHER, bool ALIGN_EPI = true, bool SP2 = true, bool REMAP64 = false>
; __device__ __forceinline__ void gemm_phase(LAS unsigned char* lds, const bf16* Ag, const bf16* Btg, const int K, const Sched& S, const Epi& E) {
;     const int tid = threadIdx.x, wid = __builtin_amdgcn_readfirstlane(tid >> 6), lane = tid & 63, wr = wid >> 2, wc = wid & 3, fr = lane & 15, fq = lane >> 4;
;     const int nt = K / BK;
;     unsigned voffA[2], voffB[2]; int RA[2], CA[2];
; #pragma unroll
;     for (int i = 0; i < 2; ++i) { int R, C; stage_rc(tid * 16 + i * 8192, R, C); const int Rb = REMAP64 ? 64 * (R >> 5) + perm32(R & 31) : (R & ~31) + perm32(R & 31);
;         voffA[i] = (unsigned)(R * K + C) * 2u; voffB[i] = (unsigned)(Rb * K + C) * 2u; RA[i] = R; CA[i] = C; }
;     const size_t kstep = (size_t)(BK * 2);
;     const size_t hstep = (size_t)HALF * K * 2;
;     const size_t hstepB = REMAP64 ? (size_t)32 * K * 2 : hstep;
;     const unsigned ldsw = (unsigned)wid * 1024u;
;     const int aoff = lds_byte(wr * 64 + fr, fq * 8), boff = lds_byte(wc * 32 + fr, fq * 8);
;     ...
;     Unit cur, nxt; int ui = 0;
;     if (!S.next(0, cur)) return;
;     f32x4 acc[2][2][4][2];
; #pragma unroll
;     for (int a = 0; a < 2; ++a)
; #pragma unroll
;         for (int b = 0; b < 2; ++b)
; #pragma unroll
;             for (int m = 0; m < 4; ++m)
; #pragma unroll
;                 for (int n = 0; n < 2; ++n) acc[a][b][m][n] = (f32x4){0.f, 0.f, 0.f, 0.f};
;     bf16x8 At[4][2], B0[2][2], B1[2][2];
;     unsigned vc[2][2], vn[2][2];
;     if (GATHER) { PG8_ROWOFFS(vc, cur); }
;     const char* cA = GATHER ? (const char*)Ag : (const char*)Ag + (size_t)cur.arow0 * K * 2; const char* cB = (const char*)Btg + S.boff(cur) * 2;
;     if constexpr (SP2) {
;         PG8_STAGE(PG8_SB(0, 0), cB, voffB); PG8_STAGE(PG8_SB(0, 1), cB + hstepB, voffB); PG8_STAGE_A(PG8_SA(0, 0), cA, vc, 0, 0); PG8_STAGE_A(PG8_SA(0, 1), cA, vc, 1, 0);
;         if (wr == 1) PG8_BAR;
;         PG8_WAIT_V(2); PG8_BAR;
;         PG8_STAGE(PG8_SB(1, 0), cB + kstep, voffB); PG8_STAGE_A(PG8_SA(1, 0), cA, vc, 0, kstep); PG8_STAGE(PG8_SB(1, 1), cB + hstepB + kstep, voffB);
;         PG8_WAIT_V(6); PG8_BAR;
.Lstag_merge:
	v_lshrrev_b32_e32 v5, 1, v0
	v_and_b32_e32 v14, 24, v5
	v_lshrrev_b32_e32 v5, 5, v0
	v_lshlrev_b32_e32 v2, 4, v0
	v_and_b32_e32 v3, 32, v0
	v_and_b32_e32 v5, 4, v5
	v_bfe_u32 v6, v0, 2, 2
	v_lshrrev_b32_e32 v4, 2, v0
	v_bitop3_b32 v10, v2, v3, 48 bitop3:0x6c
	v_and_b32_e32 v11, 64, v0
	v_or3_b32 v5, v5, v6, v14
	v_or_b32_e32 v13, 0x2000, v2
	v_bfe_u32 v12, v0, 2, 4
	v_or_b32_e32 v3, v10, v11
	v_and_or_b32 v4, v4, 64, v5
	v_lshrrev_b32_e32 v2, 7, v13
	s_movk_i32 s1, 0x70
	s_lshr_b32 s0, s18, 6
	v_lshl_or_b32 v164, v4, 11, v3
	v_and_or_b32 v2, v2, s1, v12
	v_lshrrev_b32_e32 v4, 6, v13
	s_movk_i32 s1, 0xc0
	s_ashr_i32 s9, s8, 31
	s_ashr_i32 s41, s40, 31
	v_and_or_b32 v4, v4, s1, v5
	s_lshr_b32 s1, s18, 8
	s_lshl_b32 s33, s0, 10
	s_lshl_b64 s[6:7], s[8:9], 11
	s_lshl_b64 s[10:11], s[40:41], 19
	v_readlane_b32 s12, v247, 49
	v_readlane_b32 s13, v247, 50
	s_add_u32 s42, s12, s10
	s_addc_u32 s43, s13, s11
	s_add_i32 s41, s33, 0
	s_add_i32 m0, s41, 0x10000
	v_lshl_or_b32 v168, v4, 11, v3
	global_load_lds_dwordx4 v164, s[42:43]
	s_add_i32 m0, s41, 0x12000
	s_add_u32 s10, s42, 0x10000
	global_load_lds_dwordx4 v168, s[42:43]
	s_addc_u32 s11, s43, 0
	s_add_i32 m0, s41, 0x14000
	v_readlane_b32 s12, v247, 4
	global_load_lds_dwordx4 v164, s[10:11]
	s_add_i32 m0, s41, 0x16000
	v_readlane_b32 s14, v247, 6
	v_lshrrev_b32_e32 v6, 3, v0
	v_readlane_b32 s15, v247, 7
	s_add_u32 s44, s14, s6
	v_and_or_b32 v6, v6, 48, v12
	s_addc_u32 s45, s15, s7
	s_add_i32 s56, s41, 0x2000
	v_lshl_or_b32 v162, v6, 11, v3
	global_load_lds_dwordx4 v168, s[10:11]
	s_mov_b32 m0, s41
	s_add_u32 s6, s44, 0x40000
	v_lshl_or_b32 v166, v2, 11, v3
	global_load_lds_dwordx4 v162, s[44:45]
	s_mov_b32 m0, s56
	s_addc_u32 s7, s45, 0
	s_add_i32 s57, s41, 0x4000
	global_load_lds_dwordx4 v166, s[44:45]
	s_mov_b32 m0, s57
	s_add_i32 s58, s41, 0x6000
	global_load_lds_dwordx4 v162, s[6:7]
	s_mov_b32 m0, s58
	v_mov_b32_e32 v165, 0
	global_load_lds_dwordx4 v166, s[6:7]
	v_mov_b32_e32 v169, v165
	v_mov_b32_e32 v163, v165
	v_mov_b32_e32 v167, v165
	s_cmp_eq_u32 s1, 1
	s_mov_b32 s59, 0
	v_lshl_add_u64 v[8:9], s[42:43], 0, v[164:165]
	v_lshl_add_u64 v[6:7], s[42:43], 0, v[168:169]
	v_lshl_add_u64 v[2:3], s[44:45], 0, v[162:163]
	s_cselect_b64 s[10:11], -1, 0
	s_cmp_lg_u32 s1, 1
	v_lshl_add_u64 v[4:5], s[44:45], 0, v[166:167]
	v_readlane_b32 s13, v247, 5
	s_cbranch_scc1 .LBB0_1139
	s_barrier

; template <class Epi, class Sched, bool GATHER, bool ALIGN_EPI = true, bool SP2 = true, bool REMAP64 = false>
; __device__ __forceinline__ void gemm_phase(LAS unsigned char* lds, const bf16* Ag, const bf16* Btg, const int K, const Sched& S, const Epi& E) {
;     ...
;             { const int r0_ = wr * 64 + fr; pq[0] = E.pre(cur, (r0_ < cur.nrows ? r0_ : cur.nrows - 1) + rsh, citx); }
; #pragma unroll
;             for (int gq = 0; gq < 8; ++gq) { const int ai = gq >> 2, m = gq & 3, r = ai * HALF + wr * 64 + m * 16 + fr;
;                 if (gq + 1 < 8) { const int rn = ((gq + 1) >> 2) * HALF + wr * 64 + ((gq + 1) & 3) * 16 + fr; pq[(gq + 1) & 1] = E.pre(cur, (rn < cur.nrows ? rn : cur.nrows - 1) + rsh, citx); }
;                 __builtin_amdgcn_sched_barrier(0);
;                 if (r < cur.nrows) { float v0[8], v1[8];
; #pragma unroll
;                     for (int i = 0; i < 4; ++i) { v0[i] = acc[ai][0][m][0][i]; v0[4 + i] = acc[ai][0][m][1][i]; v1[i] = acc[ai][1][m][0][i]; v1[4 + i] = acc[ai][1][m][1][i]; }
;                     if constexpr (RP) {
; #pragma unroll
;                         for (int i = 0; i < 8; ++i) { const float snd = hi ? v0[i] : v1[i];
;                             const float rcv = __builtin_bit_cast(float, __builtin_amdgcn_update_dpp(0, __builtin_bit_cast(int, snd), 0x128, 0xf, 0xf, false));
;                             if (hi) v0[i] = rcv; else v1[i] = rcv; } }
;                     E.post(cur, r + rsh, citx, v0, v1, pq[gq & 1]); }
;     __device__ __forceinline__ Pre pre(const Unit& u, int r, int cit) const { const size_t off = (size_t)(u.arow0 + r) * D + u.pn * 256 + cit; return Pre{__builtin_nontemporal_load((const v4u*)(gd + off)), __builtin_nontemporal_load((const v4u*)(gd + off + (size_t)8 * D)), __builtin_nontemporal_load ...
;     __device__ __forceinline__ void post(const Unit& u, int r, int cit, const float* v0, const float* v1, const Pre& p) const {
;         const size_t off = (size_t)(u.arow0 + r) * D + u.pn * 256 + cit; float g0[8], g1[8], m0[8], m1[8]; unpack8bf(p.g0, g0); unpack8bf(p.g1, g1); unpack8bf(p.m0, m0); unpack8bf(p.m1, m1);
; #pragma unroll
;         for (int i = 0; i < 8; ++i) { m0[i] += g0[i] * v0[i]; m1[i] += g1[i] * v1[i]; }
;         store8bf(mg + off, m0); store8bf(mg + off + (size_t)8 * D, m1);
;     }
.LBB0_1152:
	v_add_u32_e32 v130, s8, v185
	v_ashrrev_i32_e32 v131, 31, v130
	s_lshl_b32 s42, s40, 8
	v_lshlrev_b64 v[130:131], 11, v[130:131]
	s_ashr_i32 s43, s42, 31
	v_lshl_add_u64 v[130:131], v[130:131], 0, s[42:43]
	v_or_b32_e32 v130, v130, v172
	v_lshlrev_b64 v[130:131], 1, v[130:131]
	v_lshl_add_u64 v[132:133], s[50:51], 0, v[130:131]
	v_add_co_u32_e32 v134, vcc, s63, v132
	v_lshl_add_u64 v[130:131], s[20:21], 0, v[130:131]
	s_nop 0
	v_addc_co_u32_e32 v135, vcc, 0, v133, vcc
	global_load_dwordx4 v[158:161], v[132:133], off nt
	global_load_dwordx4 v[154:157], v[134:135], off nt
	v_add_co_u32_e32 v132, vcc, s63, v130
	v_add_u32_e32 v197, s8, v184
	s_nop 0
	v_addc_co_u32_e32 v133, vcc, 0, v131, vcc
	global_load_dwordx4 v[150:153], v[130:131], off nt
	global_load_dwordx4 v[146:149], v[132:133], off nt
	v_add_u32_e32 v130, v197, v186
	v_ashrrev_i32_e32 v131, 31, v130
	v_mov_b32_e32 v183, s43
	v_or_b32_e32 v182, s42, v172
	v_lshlrev_b64 v[130:131], 11, v[130:131]
	v_lshl_add_u64 v[130:131], v[130:131], 0, v[182:183]
	v_lshlrev_b64 v[130:131], 1, v[130:131]
	v_lshl_add_u64 v[132:133], s[50:51], 0, v[130:131]
	v_add_co_u32_e32 v134, vcc, 0x8000, v132
	v_lshl_add_u64 v[130:131], s[20:21], 0, v[130:131]
	s_nop 0
	v_addc_co_u32_e32 v135, vcc, 0, v133, vcc
	global_load_dwordx4 v[142:145], v[132:133], off nt
	global_load_dwordx4 v[138:141], v[134:135], off nt
	v_add_co_u32_e32 v132, vcc, 0x8000, v130
	v_add_u32_e32 v196, v197, v171
	s_nop 0
	v_addc_co_u32_e32 v133, vcc, 0, v131, vcc
	global_load_dwordx4 v[134:137], v[130:131], off nt
	s_nop 0
	global_load_dwordx4 v[130:133], v[132:133], off nt
	s_and_b64 vcc, exec, s[16:17]
	s_cbranch_vccz .LBB0_1154
	v_cndmask_b32_e64 v198, v118, v126, s[0:1]
	v_mov_b32_e32 v199, 0
	s_waitcnt vmcnt(0)
	v_lshlrev_b32_e32 v204, 16, v156
	v_lshlrev_b32_e32 v212, 16, v148
	v_mov_b32_dpp v199, v198 row_ror:8 row_mask:0xf bank_mask:0xf
	v_cndmask_b32_e64 v198, v119, v127, s[0:1]
	v_cndmask_b32_e64 v126, v126, v199, s[0:1]
	v_cndmask_b32_e64 v118, v199, v118, s[0:1]
	v_mov_b32_e32 v199, 0
	v_and_b32_e32 v156, 0xffff0000, v156
	v_and_b32_e32 v148, 0xffff0000, v148
	v_mov_b32_dpp v199, v198 row_ror:8 row_mask:0xf bank_mask:0xf
	v_cndmask_b32_e64 v198, v120, v128, s[0:1]
	v_cndmask_b32_e64 v127, v127, v199, s[0:1]
	v_cndmask_b32_e64 v119, v199, v119, s[0:1]
	v_mov_b32_e32 v199, 0
	v_lshlrev_b32_e32 v200, 16, v160
	v_and_b32_e32 v160, 0xffff0000, v160
	v_mov_b32_dpp v199, v198 row_ror:8 row_mask:0xf bank_mask:0xf
	v_cndmask_b32_e64 v198, v121, v129, s[0:1]
	v_cndmask_b32_e64 v128, v128, v199, s[0:1]
	v_cndmask_b32_e64 v120, v199, v120, s[0:1]
	v_mov_b32_e32 v199, 0
	v_lshlrev_b32_e32 v201, 16, v161
	v_and_b32_e32 v161, 0xffff0000, v161
	v_mov_b32_dpp v199, v198 row_ror:8 row_mask:0xf bank_mask:0xf
	v_cndmask_b32_e64 v198, v114, v122, s[0:1]
	v_cndmask_b32_e64 v129, v129, v199, s[0:1]
	v_cndmask_b32_e64 v121, v199, v121, s[0:1]
	v_mov_b32_e32 v199, 0
	v_lshlrev_b32_e32 v206, 16, v150
	v_and_b32_e32 v150, 0xffff0000, v150
	v_mov_b32_dpp v199, v198 row_ror:8 row_mask:0xf bank_mask:0xf
	v_cndmask_b32_e64 v198, v115, v123, s[0:1]
	v_cndmask_b32_e64 v122, v122, v199, s[0:1]
	v_cndmask_b32_e64 v114, v199, v114, s[0:1]
	v_mov_b32_e32 v199, 0
	v_fmac_f32_e32 v212, v114, v204
	v_add_u32_e32 v114, s60, v196
	v_mov_b32_dpp v199, v198 row_ror:8 row_mask:0xf bank_mask:0xf
	v_cndmask_b32_e64 v198, v116, v124, s[0:1]
	v_cndmask_b32_e64 v123, v123, v199, s[0:1]
	v_cndmask_b32_e64 v115, v199, v115, s[0:1]
	v_mov_b32_e32 v199, 0
	v_fmac_f32_e32 v148, v115, v156
	v_ashrrev_i32_e32 v115, 31, v114
	v_mov_b32_dpp v199, v198 row_ror:8 row_mask:0xf bank_mask:0xf
	v_cndmask_b32_e64 v198, v117, v125, s[0:1]
	v_cndmask_b32_e64 v124, v124, v199, s[0:1]
	v_cndmask_b32_e64 v116, v199, v116, s[0:1]
	v_mov_b32_e32 v199, 0
	v_lshlrev_b32_e32 v207, 16, v151
	v_and_b32_e32 v151, 0xffff0000, v151
	v_mov_b32_dpp v199, v198 row_ror:8 row_mask:0xf bank_mask:0xf
	v_cndmask_b32_e64 v125, v125, v199, s[0:1]
	v_cndmask_b32_e64 v117, v199, v117, s[0:1]
	v_lshlrev_b32_e32 v198, 16, v158
	v_and_b32_e32 v158, 0xffff0000, v158
	v_lshlrev_b32_e32 v199, 16, v159
	v_and_b32_e32 v159, 0xffff0000, v159
	v_lshlrev_b32_e32 v208, 16, v152
	v_and_b32_e32 v152, 0xffff0000, v152
	v_lshlrev_b32_e32 v209, 16, v153
	v_and_b32_e32 v153, 0xffff0000, v153
	v_lshlrev_b64 v[114:115], 12, v[114:115]
	v_lshlrev_b32_e32 v202, 16, v154
	v_and_b32_e32 v154, 0xffff0000, v154
	v_lshlrev_b32_e32 v205, 16, v157
	v_and_b32_e32 v157, 0xffff0000, v157
	v_lshlrev_b32_e32 v210, 16, v146
	v_and_b32_e32 v146, 0xffff0000, v146
	v_lshlrev_b32_e32 v213, 16, v149
	v_and_b32_e32 v149, 0xffff0000, v149
	v_fmac_f32_e32 v206, v126, v198
	v_fmac_f32_e32 v150, v127, v158
	v_fmac_f32_e32 v207, v128, v199
	v_fmac_f32_e32 v151, v129, v159
	v_fmac_f32_e32 v208, v122, v200
	v_fmac_f32_e32 v152, v123, v160
	v_fmac_f32_e32 v209, v124, v201
	v_fmac_f32_e32 v153, v125, v161
	v_lshl_add_u64 v[114:115], s[36:37], 0, v[114:115]
	v_lshlrev_b32_e32 v203, 16, v155
	v_and_b32_e32 v155, 0xffff0000, v155
	v_lshlrev_b32_e32 v211, 16, v147
	v_and_b32_e32 v147, 0xffff0000, v147
	v_fmac_f32_e32 v210, v118, v202
	v_fmac_f32_e32 v146, v119, v154
	v_fmac_f32_e32 v213, v116, v205
	v_fmac_f32_e32 v149, v117, v157
	v_lshl_add_u64 v[118:119], v[182:183], 1, v[114:115]
	v_cvt_pk_bf16_f32 v114, v206, v150
	v_cvt_pk_bf16_f32 v115, v207, v151
	v_cvt_pk_bf16_f32 v116, v208, v152
	v_cvt_pk_bf16_f32 v117, v209, v153
	v_fmac_f32_e32 v211, v120, v203
	v_fmac_f32_e32 v147, v121, v155
	global_store_dwordx4 v[118:119], v[114:117], off
	v_add_co_u32_e32 v118, vcc, 0x8000, v118
	s_nop 0
	v_cvt_pk_bf16_f32 v114, v210, v146
	v_cvt_pk_bf16_f32 v115, v211, v147
	v_cvt_pk_bf16_f32 v116, v212, v148
	v_cvt_pk_bf16_f32 v117, v213, v149
	v_addc_co_u32_e32 v119, vcc, 0, v119, vcc
	global_store_dwordx4 v[118:119], v[114:117], off

;     __device__ __forceinline__ size_t boff(const Unit& u) const { return (size_t)u.pn * 256 * K; }
;     __device__ __forceinline__ size_t boff(const Unit& u) const { return Dn.boff(u); }
; template <class Epi, class Sched, bool GATHER, bool ALIGN_EPI = true, bool SP2 = true, bool REMAP64 = false>
; __device__ __forceinline__ void gemm_phase(LAS unsigned char* lds, const bf16* Ag, const bf16* Btg, const int K, const Sched& S, const Epi& E) {
;     const int tid = threadIdx.x, wid = __builtin_amdgcn_readfirstlane(tid >> 6), lane = tid & 63, wr = wid >> 2, wc = wid & 3, fr = lane & 15, fq = lane >> 4;
;     const int nt = K / BK;
;     unsigned voffA[2], voffB[2]; int RA[2], CA[2];
; #pragma unroll
;     for (int i = 0; i < 2; ++i) { int R, C; stage_rc(tid * 16 + i * 8192, R, C); const int Rb = REMAP64 ? 64 * (R >> 5) + perm32(R & 31) : (R & ~31) + perm32(R & 31);
;         voffA[i] = (unsigned)(R * K + C) * 2u; voffB[i] = (unsigned)(Rb * K + C) * 2u; RA[i] = R; CA[i] = C; }
;     const size_t kstep = (size_t)(BK * 2);
;     const size_t hstep = (size_t)HALF * K * 2;
;     const size_t hstepB = REMAP64 ? (size_t)32 * K * 2 : hstep;
;     const unsigned ldsw = (unsigned)wid * 1024u;
;     const int aoff = lds_byte(wr * 64 + fr, fq * 8), boff = lds_byte(wc * 32 + fr, fq * 8);
;     ...
;     Unit cur, nxt; int ui = 0;
;     if (!S.next(0, cur)) return;
;     f32x4 acc[2][2][4][2];
; #pragma unroll
;     for (int a = 0; a < 2; ++a)
; #pragma unroll
;         for (int b = 0; b < 2; ++b)
; #pragma unroll
;             for (int m = 0; m < 4; ++m)
; #pragma unroll
;                 for (int n = 0; n < 2; ++n) acc[a][b][m][n] = (f32x4){0.f, 0.f, 0.f, 0.f};
;     bf16x8 At[4][2], B0[2][2], B1[2][2];
;     unsigned vc[2][2], vn[2][2];
;     if (GATHER) { PG8_ROWOFFS(vc, cur); }
;     const char* cA = GATHER ? (const char*)Ag : (const char*)Ag + (size_t)cur.arow0 * K * 2; const char* cB = (const char*)Btg + S.boff(cur) * 2;
;     if constexpr (SP2) {
;         PG8_STAGE(PG8_SB(0, 0), cB, voffB); PG8_STAGE(PG8_SB(0, 1), cB + hstepB, voffB); PG8_STAGE_A(PG8_SA(0, 0), cA, vc, 0, 0); PG8_STAGE_A(PG8_SA(0, 1), cA, vc, 1, 0);
;         if (wr == 1) PG8_BAR;
;         PG8_WAIT_V(2); PG8_BAR;
;         PG8_STAGE(PG8_SB(1, 0), cB + kstep, voffB); PG8_STAGE_A(PG8_SA(1, 0), cA, vc, 0, kstep); PG8_STAGE(PG8_SB(1, 1), cB + hstepB + kstep, voffB);
;         PG8_WAIT_V(6); PG8_BAR;
.Lstag_out:
	v_lshrrev_b32_e32 v5, 1, v0
	v_and_b32_e32 v14, 24, v5
	v_lshrrev_b32_e32 v5, 5, v0
	v_lshlrev_b32_e32 v2, 4, v0
	v_and_b32_e32 v3, 32, v0
	v_and_b32_e32 v5, 4, v5
	v_bfe_u32 v6, v0, 2, 2
	v_lshrrev_b32_e32 v4, 2, v0
	v_bitop3_b32 v10, v2, v3, 48 bitop3:0x6c
	v_and_b32_e32 v11, 64, v0
	v_or3_b32 v5, v5, v6, v14
	v_or_b32_e32 v13, 0x2000, v2
	v_bfe_u32 v12, v0, 2, 4
	v_or_b32_e32 v3, v10, v11
	v_and_or_b32 v4, v4, 64, v5
	v_lshrrev_b32_e32 v2, 7, v13
	s_movk_i32 s1, 0x70
	s_lshr_b32 s0, s20, 6
	v_lshl_or_b32 v164, v4, 12, v3
	v_and_or_b32 v2, v2, s1, v12
	v_lshrrev_b32_e32 v4, 6, v13
	s_movk_i32 s1, 0xc0
	s_ashr_i32 s9, s8, 31
	s_ashr_i32 s43, s42, 31
	v_and_or_b32 v4, v4, s1, v5
	s_lshr_b32 s1, s20, 8
	s_lshl_b32 s33, s0, 10
	s_lshl_b64 s[6:7], s[8:9], 12
	s_lshl_b64 s[12:13], s[42:43], 20
	v_readlane_b32 s14, v247, 51
	v_readlane_b32 s15, v247, 52
	s_add_u32 s44, s14, s12
	s_addc_u32 s45, s15, s13
	s_add_i32 s43, s33, 0
	s_add_i32 m0, s43, 0x10000
	v_lshl_or_b32 v168, v4, 12, v3
	global_load_lds_dwordx4 v164, s[44:45]
	s_add_i32 m0, s43, 0x12000
	s_add_u32 s12, s44, 0x20000
	global_load_lds_dwordx4 v168, s[44:45]
	s_addc_u32 s13, s45, 0
	s_add_i32 m0, s43, 0x14000
	v_lshrrev_b32_e32 v6, 3, v0
	global_load_lds_dwordx4 v164, s[12:13]
	s_add_i32 m0, s43, 0x16000
	s_add_u32 s52, s36, s6
	v_and_or_b32 v6, v6, 48, v12
	s_addc_u32 s53, s37, s7
	s_add_i32 s58, s43, 0x2000
	v_lshl_or_b32 v162, v6, 12, v3
	global_load_lds_dwordx4 v168, s[12:13]
	s_mov_b32 m0, s43
	s_add_u32 s6, s52, 0x80000
	v_lshl_or_b32 v166, v2, 12, v3
	global_load_lds_dwordx4 v162, s[52:53]
	s_mov_b32 m0, s58
	s_addc_u32 s7, s53, 0
	s_add_i32 s59, s43, 0x4000
	global_load_lds_dwordx4 v166, s[52:53]
	s_mov_b32 m0, s59
	s_add_i32 s60, s43, 0x6000
	global_load_lds_dwordx4 v162, s[6:7]
	s_mov_b32 m0, s60
	v_mov_b32_e32 v173, 0
	global_load_lds_dwordx4 v166, s[6:7]
	v_mov_b32_e32 v165, v173
	v_mov_b32_e32 v169, v173
	v_mov_b32_e32 v163, v173
	v_mov_b32_e32 v167, v173
	s_cmp_eq_u32 s1, 1
	s_mov_b32 s61, 0
	v_lshl_add_u64 v[8:9], s[44:45], 0, v[164:165]
	v_lshl_add_u64 v[6:7], s[44:45], 0, v[168:169]
	v_lshl_add_u64 v[2:3], s[52:53], 0, v[162:163]
	s_cselect_b64 s[12:13], -1, 0
	s_cmp_lg_u32 s1, 1
	v_lshl_add_u64 v[4:5], s[52:53], 0, v[166:167]
	s_cbranch_scc1 .LBB0_1236
	s_barrier

; template <class Epi, class Sched, bool GATHER, bool ALIGN_EPI = true, bool SP2 = true, bool REMAP64 = false>
; __device__ __forceinline__ void gemm_phase(LAS unsigned char* lds, const bf16* Ag, const bf16* Btg, const int K, const Sched& S, const Epi& E) {
;     ...
;             { const int r0_ = wr * 64 + fr; pq[0] = E.pre(cur, (r0_ < cur.nrows ? r0_ : cur.nrows - 1) + rsh, citx); }
; #pragma unroll
;             for (int gq = 0; gq < 8; ++gq) { const int ai = gq >> 2, m = gq & 3, r = ai * HALF + wr * 64 + m * 16 + fr;
;                 if (gq + 1 < 8) { const int rn = ((gq + 1) >> 2) * HALF + wr * 64 + ((gq + 1) & 3) * 16 + fr; pq[(gq + 1) & 1] = E.pre(cur, (rn < cur.nrows ? rn : cur.nrows - 1) + rsh, citx); }
;                 __builtin_amdgcn_sched_barrier(0);
;                 if (r < cur.nrows) { float v0[8], v1[8];
; #pragma unroll
;                     for (int i = 0; i < 4; ++i) { v0[i] = acc[ai][0][m][0][i]; v0[4 + i] = acc[ai][0][m][1][i]; v1[i] = acc[ai][1][m][0][i]; v1[4 + i] = acc[ai][1][m][1][i]; }
;                     if constexpr (RP) {
; #pragma unroll
;                         for (int i = 0; i < 8; ++i) { const float snd = hi ? v0[i] : v1[i];
;                             const float rcv = __builtin_bit_cast(float, __builtin_amdgcn_update_dpp(0, __builtin_bit_cast(int, snd), 0x128, 0xf, 0xf, false));
;                             if (hi) v0[i] = rcv; else v1[i] = rcv; } }
;                     E.post(cur, r + rsh, citx, v0, v1, pq[gq & 1]); }
;     __device__ __forceinline__ Pre pre(const Unit& u, int r, int cit) const { const size_t off = (size_t)(u.arow0 + r) * D + u.pn * 256 + cit; return Pre{__builtin_nontemporal_load((const f32x4*)(x + off)), __builtin_nontemporal_load((const f32x4*)(x + off + 4)), __builtin_nontemporal_load((const f3 ...
;     __device__ __forceinline__ void post(const Unit& u, int r, int cit, const float* v0, const float* v1, const Pre& p) const {
;         const size_t off = (size_t)(u.arow0 + r) * D + u.pn * 256 + cit; float a[8], b[8];
; #pragma unroll
;         for (int i = 0; i < 4; ++i) { a[i] = p.a0[i] + v0[i]; a[4 + i] = p.a1[i] + v0[4 + i]; b[i] = p.b0[i] + v1[i]; b[4 + i] = p.b1[i] + v1[4 + i]; }
;         store8bf(h + off, a); store8bf(h + off + (size_t)8 * D, b);
;     }
.LBB0_1249:
	v_add_u32_e32 v130, s8, v192
	v_ashrrev_i32_e32 v131, 31, v130
	s_lshl_b32 s44, s42, 8
	v_readlane_b32 s80, v247, 8
	s_ashr_i32 s45, s44, 31
	v_lshlrev_b64 v[130:131], 13, v[130:131]
	v_readlane_b32 s81, v247, 9
	s_lshl_b64 s[52:53], s[44:45], 2
	v_add_u32_e32 v204, s8, v191
	v_lshl_add_u64 v[130:131], s[80:81], 0, v[130:131]
	v_lshl_add_u64 v[130:131], v[130:131], 0, s[52:53]
	v_lshl_add_u64 v[130:131], v[130:131], 0, v[172:173]
	global_load_dwordx4 v[146:149], v[130:131], off offset:16 nt
	global_load_dwordx4 v[150:153], v[130:131], off nt
	v_lshl_add_u64 v[132:133], v[130:131], 0, s[22:23]
	v_add_co_u32_e32 v130, vcc, 0x10000, v130
	v_lshl_add_u64 v[188:189], v[174:175], 0, s[52:53]
	s_nop 0
	v_addc_co_u32_e32 v131, vcc, 0, v131, vcc
	global_load_dwordx4 v[154:157], v[130:131], off nt
	global_load_dwordx4 v[158:161], v[132:133], off offset:16 nt
	v_add_u32_e32 v130, v204, v193
	v_ashrrev_i32_e32 v131, 31, v130
	v_lshlrev_b64 v[130:131], 13, v[130:131]
	v_lshl_add_u64 v[138:139], v[188:189], 0, v[130:131]
	global_load_dwordx4 v[130:133], v[138:139], off offset:16 nt
	global_load_dwordx4 v[134:137], v[138:139], off nt
	v_lshl_add_u64 v[142:143], v[138:139], 0, s[22:23]
	v_add_co_u32_e32 v138, vcc, 0x10000, v138
	v_lshl_add_u64 v[186:187], s[44:45], 1, v[176:177]
	s_nop 0
	v_addc_co_u32_e32 v139, vcc, 0, v139, vcc
	global_load_dwordx4 v[138:141], v[138:139], off nt
	s_nop 0
	global_load_dwordx4 v[142:145], v[142:143], off offset:16 nt
	v_add_u32_e32 v203, v204, v171
	v_readlane_b32 s82, v247, 10
	v_readlane_b32 s83, v247, 11
	v_readlane_b32 s84, v247, 12
	v_readlane_b32 s85, v247, 13
	v_readlane_b32 s86, v247, 14
	v_readlane_b32 s87, v247, 15
	v_readlane_b32 s88, v247, 16
	v_readlane_b32 s89, v247, 17
	v_readlane_b32 s90, v247, 18
	v_readlane_b32 s91, v247, 19
	v_readlane_b32 s92, v247, 20
	v_readlane_b32 s93, v247, 21
	v_readlane_b32 s94, v247, 22
	v_readlane_b32 s95, v247, 23
	s_and_b64 vcc, exec, s[18:19]
	s_cbranch_vccz .LBB0_1251
	v_cndmask_b32_e64 v205, v118, v126, s[0:1]
	v_mov_b32_e32 v206, v173
	s_nop 1
	v_mov_b32_dpp v206, v205 row_ror:8 row_mask:0xf bank_mask:0xf
	v_cndmask_b32_e64 v205, v119, v127, s[0:1]
	v_cndmask_b32_e64 v126, v126, v206, s[0:1]
	v_cndmask_b32_e64 v118, v206, v118, s[0:1]
	v_mov_b32_e32 v206, v173
	s_waitcnt vmcnt(0)
	v_add_f32_e32 v126, v150, v126
	v_mov_b32_dpp v206, v205 row_ror:8 row_mask:0xf bank_mask:0xf
	v_cndmask_b32_e64 v205, v120, v128, s[0:1]
	v_cndmask_b32_e64 v127, v127, v206, s[0:1]
	v_cndmask_b32_e64 v119, v206, v119, s[0:1]
	v_mov_b32_e32 v206, v173
	v_add_f32_e32 v127, v151, v127
	s_nop 0
	v_mov_b32_dpp v206, v205 row_ror:8 row_mask:0xf bank_mask:0xf
	v_cndmask_b32_e64 v205, v121, v129, s[0:1]
	v_cndmask_b32_e64 v128, v128, v206, s[0:1]
	v_cndmask_b32_e64 v120, v206, v120, s[0:1]
	v_mov_b32_e32 v206, v173
	v_add_f32_e32 v128, v152, v128
	v_add_f32_e32 v120, v156, v120
	v_mov_b32_dpp v206, v205 row_ror:8 row_mask:0xf bank_mask:0xf
	v_cndmask_b32_e64 v205, v114, v122, s[0:1]
	v_cndmask_b32_e64 v129, v129, v206, s[0:1]
	v_cndmask_b32_e64 v121, v206, v121, s[0:1]
	v_mov_b32_e32 v206, v173
	v_add_f32_e32 v121, v157, v121
	s_nop 0
	v_mov_b32_dpp v206, v205 row_ror:8 row_mask:0xf bank_mask:0xf
	v_cndmask_b32_e64 v205, v115, v123, s[0:1]
	v_cndmask_b32_e64 v122, v122, v206, s[0:1]
	v_cndmask_b32_e64 v114, v206, v114, s[0:1]
	v_mov_b32_e32 v206, v173
	v_add_f32_e32 v150, v158, v114
	v_add_u32_e32 v114, s62, v203
	v_mov_b32_dpp v206, v205 row_ror:8 row_mask:0xf bank_mask:0xf
	v_cndmask_b32_e64 v205, v116, v124, s[0:1]
	v_cndmask_b32_e64 v123, v123, v206, s[0:1]
	v_cndmask_b32_e64 v115, v206, v115, s[0:1]
	v_mov_b32_e32 v206, v173
	v_add_f32_e32 v151, v159, v115
	v_ashrrev_i32_e32 v115, 31, v114
	v_mov_b32_dpp v206, v205 row_ror:8 row_mask:0xf bank_mask:0xf
	v_cndmask_b32_e64 v205, v117, v125, s[0:1]
	v_cndmask_b32_e64 v124, v124, v206, s[0:1]
	v_cndmask_b32_e64 v116, v206, v116, s[0:1]
	v_mov_b32_e32 v206, v173
	v_add_f32_e32 v122, v146, v122
	v_add_f32_e32 v123, v147, v123
	v_mov_b32_dpp v206, v205 row_ror:8 row_mask:0xf bank_mask:0xf
	v_cndmask_b32_e64 v125, v125, v206, s[0:1]
	v_cndmask_b32_e64 v117, v206, v117, s[0:1]
	v_add_f32_e32 v124, v148, v124
	v_add_f32_e32 v148, v160, v116
	v_add_f32_e32 v116, v153, v129
	v_add_f32_e32 v125, v149, v125
	v_lshlrev_b64 v[114:115], 12, v[114:115]
	v_add_f32_e32 v146, v154, v118
	v_add_f32_e32 v147, v155, v119
	v_add_f32_e32 v129, v161, v117
	v_lshl_add_u64 v[118:119], v[186:187], 0, v[114:115]
	v_cvt_pk_bf16_f32 v114, v126, v127
	v_cvt_pk_bf16_f32 v115, v128, v116
	v_cvt_pk_bf16_f32 v116, v122, v123
	v_cvt_pk_bf16_f32 v117, v124, v125
	global_store_dwordx4 v[118:119], v[114:117], off
	v_add_co_u32_e32 v118, vcc, 0x8000, v118
	s_nop 0
	v_cvt_pk_bf16_f32 v114, v146, v147
	v_cvt_pk_bf16_f32 v115, v120, v121
	v_cvt_pk_bf16_f32 v116, v150, v151
	v_cvt_pk_bf16_f32 v117, v148, v129
	v_addc_co_u32_e32 v119, vcc, 0, v119, vcc
	global_store_dwordx4 v[118:119], v[114:117], off

;     __device__ __forceinline__ size_t boff(const Unit& u) const { return (size_t)u.pn * 256 * K; }
; template <class Epi, class Sched, bool GATHER, bool ALIGN_EPI = true, bool SP2 = true, bool REMAP64 = false>
; __device__ __forceinline__ void gemm_phase(LAS unsigned char* lds, const bf16* Ag, const bf16* Btg, const int K, const Sched& S, const Epi& E) {
;     const int tid = threadIdx.x, wid = __builtin_amdgcn_readfirstlane(tid >> 6), lane = tid & 63, wr = wid >> 2, wc = wid & 3, fr = lane & 15, fq = lane >> 4;
;     const int nt = K / BK;
;     unsigned voffA[2], voffB[2]; int RA[2], CA[2];
; #pragma unroll
;     for (int i = 0; i < 2; ++i) { int R, C; stage_rc(tid * 16 + i * 8192, R, C); const int Rb = REMAP64 ? 64 * (R >> 5) + perm32(R & 31) : (R & ~31) + perm32(R & 31);
;         voffA[i] = (unsigned)(R * K + C) * 2u; voffB[i] = (unsigned)(Rb * K + C) * 2u; RA[i] = R; CA[i] = C; }
;     const size_t kstep = (size_t)(BK * 2);
;     const size_t hstep = (size_t)HALF * K * 2;
;     const size_t hstepB = REMAP64 ? (size_t)32 * K * 2 : hstep;
;     const unsigned ldsw = (unsigned)wid * 1024u;
;     const int aoff = lds_byte(wr * 64 + fr, fq * 8), boff = lds_byte(wc * 32 + fr, fq * 8);
;     ...
;     Unit cur, nxt; int ui = 0;
;     if (!S.next(0, cur)) return;
;     f32x4 acc[2][2][4][2];
; #pragma unroll
;     for (int a = 0; a < 2; ++a)
; #pragma unroll
;         for (int b = 0; b < 2; ++b)
; #pragma unroll
;             for (int m = 0; m < 4; ++m)
; #pragma unroll
;                 for (int n = 0; n < 2; ++n) acc[a][b][m][n] = (f32x4){0.f, 0.f, 0.f, 0.f};
;     bf16x8 At[4][2], B0[2][2], B1[2][2];
;     unsigned vc[2][2], vn[2][2];
;     if (GATHER) { PG8_ROWOFFS(vc, cur); }
;     const char* cA = GATHER ? (const char*)Ag : (const char*)Ag + (size_t)cur.arow0 * K * 2; const char* cB = (const char*)Btg + S.boff(cur) * 2;
;     if constexpr (SP2) {
;         PG8_STAGE(PG8_SB(0, 0), cB, voffB); PG8_STAGE(PG8_SB(0, 1), cB + hstepB, voffB); PG8_STAGE_A(PG8_SA(0, 0), cA, vc, 0, 0); PG8_STAGE_A(PG8_SA(0, 1), cA, vc, 1, 0);
;         if (wr == 1) PG8_BAR;
;         PG8_WAIT_V(2); PG8_BAR;
; __global__ void __launch_bounds__(NTHR, 2) fwd(Args args) {
;     ...
;     if (IN(PH_PLE)) { pg8::DenseOrder S; S.init(T, D, D, F.G, (int)blockIdx.x); EpiPle E{PP, H}; pg8::gemm_phase<EpiPle, pg8::DenseOrder, false, true, true, true>(F.lds + RING_OFF, N1, WPLEG, D, S, E); }
.LBB0_1720:
	s_andn2_b64 vcc, exec, s[0:1]
	s_cbranch_vccnz .LBB0_1756
	v_readlane_b32 s98, v247, 2
	s_nop 3
	s_and_b32 s98, s98, 4
	s_cmp_eq_u32 s98, 0
	s_cbranch_scc1 .Lstag_ple
	s_sleep 127
	s_sleep 127
.Lstag_ple:
	v_lshrrev_b32_e32 v5, 1, v0
	v_and_b32_e32 v13, 24, v5
	v_lshrrev_b32_e32 v5, 5, v0
	v_lshlrev_b32_e32 v2, 4, v0
	v_and_b32_e32 v1, 32, v0
	v_and_b32_e32 v5, 4, v5
	v_bfe_u32 v6, v0, 2, 2
	v_lshrrev_b32_e32 v3, 2, v0
	v_bitop3_b32 v1, v2, v1, 48 bitop3:0x6c
	v_and_b32_e32 v10, 64, v0
	v_or3_b32 v5, v5, v6, v13
	v_or_b32_e32 v12, 0x2000, v2
	v_bfe_u32 v11, v0, 2, 4
	v_or_b32_e32 v4, v1, v10
	v_and_or_b32 v3, v3, 64, v5
	v_lshrrev_b32_e32 v2, 7, v12
	s_movk_i32 s1, 0x70
	s_lshr_b32 s0, s22, 6
	v_lshl_or_b32 v166, v3, 12, v4
	v_and_or_b32 v2, v2, s1, v11
	v_lshrrev_b32_e32 v3, 6, v12
	s_movk_i32 s1, 0xc0
	s_ashr_i32 s9, s8, 31
	s_ashr_i32 s41, s40, 31
	v_and_or_b32 v3, v3, s1, v5
	s_lshr_b32 s1, s22, 8
	s_lshl_b32 s33, s0, 10
	s_lshl_b64 s[6:7], s[8:9], 12
	s_lshl_b64 s[14:15], s[40:41], 20
	v_readlane_b32 s9, v247, 53
	s_add_u32 s42, s9, s14
	v_readlane_b32 s9, v247, 54
	s_addc_u32 s43, s9, s15
	s_add_i32 s41, s33, 0
	s_add_i32 m0, s41, 0x10000
	v_lshl_or_b32 v170, v3, 12, v4
	global_load_lds_dwordx4 v166, s[42:43]
	s_add_i32 m0, s41, 0x12000
	s_add_u32 s14, s42, 0x20000
	global_load_lds_dwordx4 v170, s[42:43]
	s_addc_u32 s15, s43, 0
	s_add_i32 m0, s41, 0x14000
	v_lshrrev_b32_e32 v6, 3, v0
	global_load_lds_dwordx4 v166, s[14:15]
	s_add_i32 m0, s41, 0x16000
	s_add_u32 s44, s34, s6
	v_and_or_b32 v6, v6, 48, v11
	s_addc_u32 s45, s35, s7
	s_add_i32 s50, s41, 0x2000
	v_lshl_or_b32 v164, v6, 12, v4
	global_load_lds_dwordx4 v170, s[14:15]
	s_mov_b32 m0, s41
	s_add_u32 s6, s44, 0x80000
	v_lshl_or_b32 v168, v2, 12, v4
	global_load_lds_dwordx4 v164, s[44:45]
	s_mov_b32 m0, s50
	s_addc_u32 s7, s45, 0
	s_add_i32 s51, s41, 0x4000
	global_load_lds_dwordx4 v168, s[44:45]
	s_mov_b32 m0, s51
	s_add_i32 s52, s41, 0x6000
	global_load_lds_dwordx4 v164, s[6:7]
	s_mov_b32 m0, s52
	v_mov_b32_e32 v167, 0
	global_load_lds_dwordx4 v168, s[6:7]
	v_mov_b32_e32 v171, v167
	v_mov_b32_e32 v165, v167
	v_mov_b32_e32 v169, v167
	s_cmp_eq_u32 s1, 1
	s_mov_b32 s53, 0
	v_lshl_add_u64 v[8:9], s[42:43], 0, v[166:167]
	v_lshl_add_u64 v[6:7], s[42:43], 0, v[170:171]
	v_lshl_add_u64 v[2:3], s[44:45], 0, v[164:165]
	s_cselect_b64 s[14:15], -1, 0
	s_cmp_lg_u32 s1, 1
	v_lshl_add_u64 v[4:5], s[44:45], 0, v[168:169]
	s_cbranch_scc1 .LBB0_1723
	s_barrier

;     __device__ __forceinline__ Pre pre(const Unit& u, int r, int cit) const { const size_t off = (size_t)(u.arow0 + r) * D + u.pn * 256 + cit; return Pre{__builtin_nontemporal_load((const v4u*)(gp + off)), __builtin_nontemporal_load((const v4u*)(gp + off + (size_t)8 * D))}; }
;     __device__ __forceinline__ Pre pre(const Unit& u, int r, int cit) const { const size_t off = (size_t)(u.arow0 + r) * D + u.pn * 256 + cit; return Pre{__builtin_nontemporal_load((const v4u*)(gd + off)), __builtin_nontemporal_load((const v4u*)(gd + off + (size_t)8 * D)), __builtin_nontemporal_load((const v4u*)(mp + off)), __builtin_nontemporal_load((const v4u*)(mp + off + (size_t)8 * D))}; }
; template <class Epi, class Sched, bool GATHER, bool ALIGN_EPI = true, bool SP2 = true, bool REMAP64 = false>
; __device__ __forceinline__ void gemm_phase(LAS unsigned char* lds, const bf16* Ag, const bf16* Btg, const int K, const Sched& S, const Epi& E) {
;     ...
;             { const int r0_ = wr * 64 + fr; pq[0] = E.pre(cur, (r0_ < cur.nrows ? r0_ : cur.nrows - 1) + rsh, citx); }
; #pragma unroll
;             for (int gq = 0; gq < 8; ++gq) { const int ai = gq >> 2, m = gq & 3, r = ai * HALF + wr * 64 + m * 16 + fr;
;                 if (gq + 1 < 8) { const int rn = ((gq + 1) >> 2) * HALF + wr * 64 + ((gq + 1) & 3) * 16 + fr; pq[(gq + 1) & 1] = E.pre(cur, (rn < cur.nrows ? rn : cur.nrows - 1) + rsh, citx); }
;     __device__ __forceinline__ Pre pre(const Unit& u, int r, int cit) const { const size_t off = (size_t)(u.arow0 + r) * D + u.pn * 256 + cit;
;         return Pre{__builtin_nontemporal_load((const v4u*)(pp + off)), __builtin_nontemporal_load((const v4u*)(pp + off + (size_t)8 * D)), *(const v4u*)(h + off), *(const v4u*)(h + off + (size_t)8 * D)}; }
.LBB0_1736:
	v_add_u32_e32 v128, s8, v189
	v_ashrrev_i32_e32 v129, 31, v128
	s_lshl_b32 s42, s40, 8
	v_lshlrev_b64 v[128:129], 11, v[128:129]
	s_ashr_i32 s43, s42, 31
	v_lshl_add_u64 v[128:129], v[128:129], 0, s[42:43]
	v_or_b32_e32 v128, v128, v172
	v_lshlrev_b64 v[128:129], 1, v[128:129]
	v_lshl_add_u64 v[130:131], s[36:37], 0, v[128:129]
	v_add_co_u32_e32 v132, vcc, s57, v130
	v_lshl_add_u64 v[128:129], s[4:5], 0, v[128:129]
	s_nop 0
	v_addc_co_u32_e32 v133, vcc, 0, v131, vcc
	global_load_dwordx4 v[156:159], v[130:131], off nt
	global_load_dwordx4 v[144:147], v[132:133], off nt
	v_add_co_u32_e32 v130, vcc, s57, v128
	v_add_u32_e32 v201, s8, v188
	s_nop 0
	v_addc_co_u32_e32 v131, vcc, 0, v129, vcc
	global_load_dwordx4 v[152:155], v[128:129], off
	global_load_dwordx4 v[148:151], v[130:131], off
	v_add_u32_e32 v128, v201, v190
	v_ashrrev_i32_e32 v129, 31, v128
	v_mov_b32_e32 v187, s43
	v_or_b32_e32 v186, s42, v172
	v_lshlrev_b64 v[128:129], 11, v[128:129]
	v_lshl_add_u64 v[128:129], v[128:129], 0, v[186:187]
	v_lshlrev_b64 v[132:133], 1, v[128:129]
	v_lshl_add_u64 v[128:129], s[36:37], 0, v[132:133]
	v_add_co_u32_e32 v130, vcc, 0x8000, v128
	v_lshl_add_u64 v[132:133], s[4:5], 0, v[132:133]
	s_nop 0
	v_addc_co_u32_e32 v131, vcc, 0, v129, vcc
	v_add_co_u32_e32 v134, vcc, 0x8000, v132
	global_load_dwordx4 v[140:143], v[128:129], off nt
	s_nop 0
	global_load_dwordx4 v[128:131], v[130:131], off nt
	v_addc_co_u32_e32 v135, vcc, 0, v133, vcc
	global_load_dwordx4 v[136:139], v[132:133], off
	s_nop 0
	global_load_dwordx4 v[132:135], v[134:135], off
	v_lshl_add_u64 v[184:185], s[42:43], 1, v[174:175]
	v_add_u32_e32 v200, v201, v161
	s_and_b64 vcc, exec, s[20:21]
	s_cbranch_vccz .LBB0_1738
; __device__ __forceinline__ float sigmoidf_(float x) { return __builtin_amdgcn_rcpf(1.0f + __builtin_amdgcn_exp2f(-1.4426950408889634f * x)); }
; __device__ __forceinline__ void unpack8bf(const v4u o, float* v) { v[0] = bflo(o.x); v[1] = bfhi(o.x); v[2] = bflo(o.y); v[3] = bfhi(o.y); v[4] = bflo(o.z); v[5] = bfhi(o.z); v[6] = bflo(o.w); v[7] = bfhi(o.w); }
; template <class Epi, class Sched, bool GATHER, bool ALIGN_EPI = true, bool SP2 = true, bool REMAP64 = false>
; __device__ __forceinline__ void gemm_phase(LAS unsigned char* lds, const bf16* Ag, const bf16* Btg, const int K, const Sched& S, const Epi& E) {
;     ...
;                     if constexpr (RP) {
; #pragma unroll
;                         for (int i = 0; i < 8; ++i) { const float snd = hi ? v0[i] : v1[i];
;                             const float rcv = __builtin_bit_cast(float, __builtin_amdgcn_update_dpp(0, __builtin_bit_cast(int, snd), 0x128, 0xf, 0xf, false));
;                             if (hi) v0[i] = rcv; else v1[i] = rcv; } }
;                     E.post(cur, r + rsh, citx, v0, v1, pq[gq & 1]); }
;     __device__ __forceinline__ void post(const Unit& u, int r, int cit, const float* v0, const float* v1, const Pre& p) const {
;         const size_t off = (size_t)(u.arow0 + r) * D + u.pn * 256 + cit; float p0[8], p1[8], a[8], b[8]; unpack8bf(p.p0, p0); unpack8bf(p.p1, p1); unpack8bf(p.h0, a); unpack8bf(p.h1, b);
; #pragma unroll
;         for (int i = 0; i < 8; ++i) { a[i] += sigmoidf_(v0[i]) * p0[i]; b[i] += sigmoidf_(v1[i]) * p1[i]; }
;         store8bf(h + off, a); store8bf(h + off + (size_t)8 * D, b);
;     }
	v_cndmask_b32_e64 v202, v116, v124, s[0:1]
	v_mov_b32_e32 v203, 0
	s_nop 1
	v_mov_b32_dpp v203, v202 row_ror:8 row_mask:0xf bank_mask:0xf
	v_cndmask_b32_e64 v202, v117, v125, s[0:1]
	v_cndmask_b32_e64 v124, v124, v203, s[0:1]
	v_cndmask_b32_e64 v116, v203, v116, s[0:1]
	v_mov_b32_e32 v203, 0
	s_nop 1
	v_mov_b32_dpp v203, v202 row_ror:8 row_mask:0xf bank_mask:0xf
	v_cndmask_b32_e64 v202, v118, v126, s[0:1]
	v_cndmask_b32_e64 v125, v125, v203, s[0:1]
	v_cndmask_b32_e64 v203, v203, v117, s[0:1]
	v_mov_b32_e32 v117, 0
	s_nop 1
	v_mov_b32_dpp v117, v202 row_ror:8 row_mask:0xf bank_mask:0xf
	v_cndmask_b32_e64 v202, v119, v127, s[0:1]
	v_cndmask_b32_e64 v126, v126, v117, s[0:1]
	v_cndmask_b32_e64 v204, v117, v118, s[0:1]
	v_mov_b32_e32 v117, 0
	v_cndmask_b32_e64 v118, v112, v120, s[0:1]
	s_nop 0
	v_mov_b32_dpp v117, v202 row_ror:8 row_mask:0xf bank_mask:0xf
	v_cndmask_b32_e64 v127, v127, v117, s[0:1]
	v_cndmask_b32_e64 v202, v117, v119, s[0:1]
	v_mov_b32_e32 v117, 0
	s_waitcnt vmcnt(0)
	v_and_b32_e32 v119, 0xffff0000, v152
	v_mov_b32_dpp v117, v118 row_ror:8 row_mask:0xf bank_mask:0xf
	v_cndmask_b32_e64 v118, v113, v121, s[0:1]
	v_cndmask_b32_e64 v206, v117, v112, s[0:1]
	v_mov_b32_e32 v112, 0
	v_cndmask_b32_e64 v205, v120, v117, s[0:1]
	v_cndmask_b32_e64 v117, v114, v122, s[0:1]
	v_mov_b32_dpp v112, v118 row_ror:8 row_mask:0xf bank_mask:0xf
	v_cndmask_b32_e64 v207, v121, v112, s[0:1]
	v_cndmask_b32_e64 v208, v112, v113, s[0:1]
	v_mov_b32_e32 v112, 0
	v_cndmask_b32_e64 v113, v115, v123, s[0:1]
	v_lshlrev_b32_e32 v118, 16, v152
	v_mov_b32_dpp v112, v117 row_ror:8 row_mask:0xf bank_mask:0xf
	v_cndmask_b32_e64 v210, v112, v114, s[0:1]
	v_mul_f32_e32 v114, 0xbfb8aa3b, v124
	v_exp_f32_e32 v114, v114
	v_cndmask_b32_e64 v209, v122, v112, s[0:1]
	v_mov_b32_e32 v112, 0
	v_and_b32_e32 v117, 0xffff0000, v156
	v_and_b32_e32 v121, 0xffff0000, v157
	v_mov_b32_dpp v112, v113 row_ror:8 row_mask:0xf bank_mask:0xf
	v_mul_f32_e32 v113, 0xbfb8aa3b, v116
	v_cndmask_b32_e64 v211, v123, v112, s[0:1]
	v_cndmask_b32_e64 v212, v112, v115, s[0:1]
	v_add_f32_e32 v112, 1.0, v114
	v_exp_f32_e32 v113, v113
	v_mul_f32_e32 v114, 0xbfb8aa3b, v125
	v_exp_f32_e32 v115, v114
	v_rcp_f32_e32 v112, v112
	v_add_f32_e32 v113, 1.0, v113
	v_rcp_f32_e32 v114, v113
	v_add_f32_e32 v113, 1.0, v115
	v_mul_f32_e32 v115, 0xbfb8aa3b, v203
	v_exp_f32_e32 v115, v115
	v_rcp_f32_e32 v113, v113
	v_lshlrev_b32_e32 v116, 16, v156
	v_lshlrev_b32_e32 v122, 16, v153
	v_add_f32_e32 v115, 1.0, v115
	v_rcp_f32_e32 v115, v115
	v_pk_fma_f32 v[112:113], v[112:113], v[116:117], v[118:119]
	v_mul_f32_e32 v118, 0xbfb8aa3b, v126
	v_lshlrev_b32_e32 v116, 16, v144
	v_and_b32_e32 v117, 0xffff0000, v144
	v_exp_f32_e32 v120, v118
	v_lshlrev_b32_e32 v118, 16, v148
	v_and_b32_e32 v119, 0xffff0000, v148
	v_pk_fma_f32 v[116:117], v[114:115], v[116:117], v[118:119]
	v_mul_f32_e32 v115, 0xbfb8aa3b, v204
	v_exp_f32_e32 v115, v115
	v_mul_f32_e32 v118, 0xbfb8aa3b, v127
	v_exp_f32_e32 v119, v118
	v_add_f32_e32 v114, 1.0, v120
	v_add_f32_e32 v115, 1.0, v115
	v_rcp_f32_e32 v118, v115
	v_add_f32_e32 v115, 1.0, v119
	v_mul_f32_e32 v119, 0xbfb8aa3b, v202
	v_exp_f32_e32 v119, v119
	v_rcp_f32_e32 v114, v114
	v_rcp_f32_e32 v115, v115
	v_lshlrev_b32_e32 v120, 16, v157
	v_add_f32_e32 v119, 1.0, v119
	v_rcp_f32_e32 v119, v119
	v_and_b32_e32 v123, 0xffff0000, v153
	v_pk_fma_f32 v[114:115], v[114:115], v[120:121], v[122:123]
	v_mul_f32_e32 v122, 0xbfb8aa3b, v205
	v_lshlrev_b32_e32 v120, 16, v145
	v_and_b32_e32 v121, 0xffff0000, v145
	v_exp_f32_e32 v124, v122
	v_lshlrev_b32_e32 v122, 16, v149
	v_and_b32_e32 v123, 0xffff0000, v149
	v_pk_fma_f32 v[118:119], v[118:119], v[120:121], v[122:123]
	v_mul_f32_e32 v121, 0xbfb8aa3b, v206
	v_exp_f32_e32 v121, v121
	v_mul_f32_e32 v122, 0xbfb8aa3b, v207
	v_exp_f32_e32 v123, v122
	v_add_f32_e32 v120, 1.0, v124
	v_add_f32_e32 v121, 1.0, v121
	v_rcp_f32_e32 v122, v121
	v_add_f32_e32 v121, 1.0, v123
	v_mul_f32_e32 v123, 0xbfb8aa3b, v208
	v_exp_f32_e32 v123, v123
	v_rcp_f32_e32 v120, v120
	v_rcp_f32_e32 v121, v121
	v_lshlrev_b32_e32 v124, 16, v158
	v_add_f32_e32 v123, 1.0, v123
	v_rcp_f32_e32 v123, v123
	v_and_b32_e32 v125, 0xffff0000, v158
	v_lshlrev_b32_e32 v126, 16, v154
	v_and_b32_e32 v127, 0xffff0000, v154
	v_pk_fma_f32 v[120:121], v[120:121], v[124:125], v[126:127]
	v_mul_f32_e32 v126, 0xbfb8aa3b, v209
	v_lshlrev_b32_e32 v124, 16, v146
	v_and_b32_e32 v125, 0xffff0000, v146
	v_exp_f32_e32 v144, v126
	v_lshlrev_b32_e32 v126, 16, v150
	v_and_b32_e32 v127, 0xffff0000, v150
	v_pk_fma_f32 v[122:123], v[122:123], v[124:125], v[126:127]
	v_mul_f32_e32 v125, 0xbfb8aa3b, v210
	v_exp_f32_e32 v125, v125
	v_mul_f32_e32 v126, 0xbfb8aa3b, v211
	v_exp_f32_e32 v127, v126
	v_add_f32_e32 v124, 1.0, v144
	v_add_f32_e32 v125, 1.0, v125
	v_rcp_f32_e32 v126, v125
	v_add_f32_e32 v125, 1.0, v127
	v_mul_f32_e32 v127, 0xbfb8aa3b, v212
	v_exp_f32_e32 v127, v127
	v_rcp_f32_e32 v124, v124
	v_rcp_f32_e32 v125, v125
	v_lshlrev_b32_e32 v144, 16, v159
	v_add_f32_e32 v127, 1.0, v127
	v_rcp_f32_e32 v127, v127
	v_and_b32_e32 v145, 0xffff0000, v159
	v_lshlrev_b32_e32 v148, 16, v155
	v_and_b32_e32 v149, 0xffff0000, v155
	v_pk_fma_f32 v[124:125], v[124:125], v[144:145], v[148:149]
	v_lshlrev_b32_e32 v144, 16, v147
	v_and_b32_e32 v145, 0xffff0000, v147
	v_lshlrev_b32_e32 v146, 16, v151
	v_and_b32_e32 v147, 0xffff0000, v151
	v_pk_fma_f32 v[126:127], v[126:127], v[144:145], v[146:147]
	v_add_u32_e32 v144, s54, v200
	v_ashrrev_i32_e32 v145, 31, v144
	v_lshlrev_b64 v[144:145], 12, v[144:145]
	v_lshl_add_u64 v[144:145], v[184:185], 0, v[144:145]
	v_cvt_pk_bf16_f32 v112, v112, v113
	v_cvt_pk_bf16_f32 v113, v114, v115
	v_cvt_pk_bf16_f32 v114, v120, v121
	v_cvt_pk_bf16_f32 v115, v124, v125
	global_store_dwordx4 v[144:145], v[112:115], off
	s_nop 1
	v_cvt_pk_bf16_f32 v112, v116, v117
	v_add_co_u32_e32 v116, vcc, 0x8000, v144
	v_cvt_pk_bf16_f32 v113, v118, v119
	v_cvt_pk_bf16_f32 v114, v122, v123
	v_cvt_pk_bf16_f32 v115, v126, v127
	v_addc_co_u32_e32 v117, vcc, 0, v145, vcc
	global_store_dwordx4 v[116:117], v[112:115], off

; __global__ void __launch_bounds__(NTHR, 2) fwd(Args args) {
	.amdhsa_kernel _Z3fwd4Args
		.amdhsa_group_segment_fixed_size 0
		.amdhsa_private_segment_fixed_size 0
		.amdhsa_kernarg_size 488
		.amdhsa_user_sgpr_count 2
		.amdhsa_user_sgpr_dispatch_ptr 0
		.amdhsa_user_sgpr_queue_ptr 0
		.amdhsa_user_sgpr_kernarg_segment_ptr 1
		.amdhsa_user_sgpr_dispatch_id 0
		.amdhsa_user_sgpr_kernarg_preload_length 0
		.amdhsa_user_sgpr_kernarg_preload_offset 0
		.amdhsa_user_sgpr_private_segment_size 0
		.amdhsa_uses_dynamic_stack 0
		.amdhsa_enable_private_segment 0
		.amdhsa_system_sgpr_workgroup_id_x 1
		.amdhsa_system_sgpr_workgroup_id_y 0
		.amdhsa_system_sgpr_workgroup_id_z 0
		.amdhsa_system_sgpr_workgroup_info 0
		.amdhsa_system_vgpr_workitem_id 0
		.amdhsa_next_free_vgpr 248
		.amdhsa_next_free_sgpr 100
		.amdhsa_accum_offset 248
		.amdhsa_reserve_vcc 1
		.amdhsa_float_round_mode_32 0
		.amdhsa_float_round_mode_16_64 0
		.amdhsa_float_denorm_mode_32 3
		.amdhsa_float_denorm_mode_16_64 3
		.amdhsa_dx10_clamp 1
		.amdhsa_ieee_mode 1
		.amdhsa_fp16_overflow 0
		.amdhsa_tg_split 0
		.amdhsa_exception_fp_ieee_invalid_op 0
		.amdhsa_exception_fp_denorm_src 0
		.amdhsa_exception_fp_ieee_div_zero 0
		.amdhsa_exception_fp_ieee_overflow 0
		.amdhsa_exception_fp_ieee_underflow 0
		.amdhsa_exception_fp_ieee_inexact 0
		.amdhsa_exception_int_div_zero 0
	.end_amdhsa_kernel

; __global__ void __launch_bounds__(NTHR, 2) fwd(Args args) {
amdhsa.kernels:
  - .agpr_count:     0
    .args:
      - .offset:         0
        .size:           232
        .value_kind:     by_value
      - .offset:         232
        .size:           4
        .value_kind:     hidden_block_count_x
      - .offset:         236
        .size:           4
        .value_kind:     hidden_block_count_y
      - .offset:         240
        .size:           4
        .value_kind:     hidden_block_count_z
      - .offset:         244
        .size:           2
        .value_kind:     hidden_group_size_x
      - .offset:         246
        .size:           2
        .value_kind:     hidden_group_size_y
      - .offset:         248
        .size:           2
        .value_kind:     hidden_group_size_z
      - .offset:         250
        .size:           2
        .value_kind:     hidden_remainder_x
      - .offset:         252
        .size:           2
        .value_kind:     hidden_remainder_y
      - .offset:         254
        .size:           2
        .value_kind:     hidden_remainder_z
      - .offset:         272
        .size:           8
        .value_kind:     hidden_global_offset_x
      - .offset:         280
        .size:           8
        .value_kind:     hidden_global_offset_y
      - .offset:         288
        .size:           8
        .value_kind:     hidden_global_offset_z
      - .offset:         296
        .size:           2
        .value_kind:     hidden_grid_dims
      - .offset:         352
        .size:           4
        .value_kind:     hidden_dynamic_lds_size
    .group_segment_fixed_size: 0
    .kernarg_segment_align: 8
    .kernarg_segment_size: 488
    .language:       OpenCL C
    .language_version:
      - 2
      - 0
    .max_flat_workgroup_size: 512
    .name:           _Z3fwd4Args
    .private_segment_fixed_size: 0
    .sgpr_count:     106
    .sgpr_spill_count: 113
    .symbol:         _Z3fwd4Args.kd
    .uniform_work_group_size: 1
    .uses_dynamic_stack: false
    .vgpr_count:     248
    .vgpr_spill_count: 0
    .wavefront_size: 64
